# barrier elision in P2 on top of the stacked version (unit-prologue barrier and chunk-end barrier implied by the queue pop's two barriers)
# speedup vs baseline: 1.0046x; 1.0046x over previous
; template <bool ISA>
; __device__ __forceinline__ void attn_unit(const Params& p, unsigned char* smem, int b, int hh, int blk) {
;     ...
;     if (ISA) { const int g = hh >> 2; kbase = p.ka + (size_t)(b * TT) * 128 + g * 64; ldk = 128; vbase = p.vta + (size_t)((b * 2 + g) * 64) * TT; }
;     else { kbase = p.kb + (size_t)(b * TT) * 512 + hh * 64; ldk = 512; vbase = p.vtb + (size_t)((b * 8 + hh) * 64) * TT; }
;     float* rpbl = (float*)(smem + 49152);
;     const float M2 = p.attm[ISA ? hh : 8 + hh], negM2 = -M2;
;     const int qt0 = ISA ? blk * 128 + wid * 32 : blk * 128 + wid * 16;
;     bf16x8 qf[NQ][2];
;     {
;         const bf16_t* qsrc = ISA ? p.qa : p.qb;
; #pragma unroll
;         for (int q = 0; q < NQ; ++q)
; #pragma unroll
;             for (int ks = 0; ks < 2; ++ks)
;                 qf[q][ks] = *(const bf16x8*)(qsrc + (size_t)(b * TT + qt0 + q * QSTR + l15) * 512 + hh * 64 + ks * 32 + gq * 8);
;     }
;     f32x4 osum[NQ]; f32x4 o[NQ][4];
; #pragma unroll
;     for (int q = 0; q < NQ; ++q) {
;         const float l0 = ISA ? __builtin_amdgcn_exp2f(p.sink[hh] * L2E - M2) : 0.f;
;         osum[q] = (f32x4){l0, l0, l0, l0};
; #pragma unroll
;         for (int df = 0; df < 4; ++df) o[q][df] = (f32x4){0.f, 0.f, 0.f, 0.f};
;     }
;     const int qcol = wid * 16 + l15;
;     int cs = wid * 16 - 8; cs = cs < 0 ? 0 : (cs > 32 ? 32 : cs);
;     int wstart = qcol - 8; wstart = wstart < 0 ? 0 : (wstart > 48 ? 48 : wstart);
;     NaConst nc;
; #pragma unroll
; __device__ void phase2(const Params& p, unsigned char* smem, unsigned* qw) {
;     ...
;         const int q = (x + aq) & 7;
;         __syncthreads();
;         if (threadIdx.x == 0) *qslot = (int)__hip_atomic_fetch_add(qw + (take_conv ? 0 : 64 * (2 + q)), 1u, __ATOMIC_RELAXED, __HIP_MEMORY_SCOPE_AGENT);
;         __syncthreads();
;         const int item = *qslot;
;         if (take_conv) {
;             if (item >= nchunks) { conv_left = false; continue; }
;             conv_jobs_deep(p, smem, item * 16, item * 16 + 16);
;         } else {
;             if (item >= 256) { if (++aq == 8) att_left = false; continue; }
;             if (item < 128) {
;                 const int u = item * 2 + sub;
;                 attn_unit<true>(p, sm, q >> 1, (q & 1) * 4 + (u & 3), u >> 2);
;             } else {
;                 const int j = item - 128;
;                 attn_unit<false>(p, sm, j >> 5, q, (j & 31) * 2 + sub);
.LBB0_377:
	s_or_b64 exec, exec, s[6:7]
	s_waitcnt lgkmcnt(0)
	s_barrier
	s_waitcnt vmcnt(0)
	ds_read_b32 v2, v118
	s_xor_b64 s[6:7], s[0:1], -1
	s_mov_b64 s[0:1], -1
	s_and_b64 vcc, exec, s[6:7]
	s_waitcnt lgkmcnt(0)
	v_readfirstlane_b32 s4, v2
	s_cbranch_vccz .LBB0_429
	s_cmpk_lt_i32 s4, 0x100
	s_cbranch_scc0 .LBB0_426
	s_cmpk_gt_i32 s4, 0x7f
	s_cbranch_scc0 .LBB0_401
	s_add_i32 s0, s4, 0xffffff80
	s_lshr_b32 s24, s0, 5
	s_lshl_b32 s76, s5, 6
	s_lshl_b32 s6, s24, 9
	s_lshl_b32 s0, s4, 1
	s_or_b32 s6, s6, s76
	s_and_b32 s0, s0, 62
	s_mulk_i32 s6, 0x2100
	s_mov_b32 s7, s77
	v_add_u32_e32 v21, s0, v1
	v_mov_b32_e32 v30, v0
	s_lshl_b64 s[6:7], s[6:7], 1
	v_readlane_b32 s9, v248, 26
	v_lshlrev_b32_e32 v101, 1, v21
	v_bfe_u32 v31, v30, 6, 2
	s_add_u32 s6, s9, s6
	v_readlane_b32 s9, v248, 28
	v_add_u32_e32 v19, -4, v101
	s_addc_u32 s7, s9, s7
	s_or_b32 s23, s5, 8
	v_lshlrev_b32_e32 v20, 4, v31
	v_min_i32_e32 v2, 0x77, v19
	s_mul_i32 s8, s24, 0x2100
	s_lshl_b32 s9, s23, 2
	v_lshl_or_b32 v100, v21, 7, v20
	v_lshlrev_b32_e32 v22, 6, v2
	v_mov_b32_e32 v4, s9
	v_add_u32_e32 v2, s8, v100
	s_lshl_b32 s10, s5, 7
	v_readlane_b32 s8, v248, 9
	v_and_b32_e32 v112, 15, v30
	v_readlane_b32 s9, v248, 10
	s_add_u32 s8, s8, s10
	v_or_b32_e32 v6, v2, v112
	s_addc_u32 s9, s9, 0
	v_and_b32_e32 v98, 48, v30
	v_lshl_add_u64 v[8:9], s[8:9], 0, v[98:99]
	v_ashrrev_i32_e32 v7, 31, v6
	v_readlane_b32 s8, v248, 20
	s_mul_i32 s0, s24, 0x420000
	s_mov_b32 s1, s77
	v_lshlrev_b64 v[2:3], 10, v[6:7]
	v_readlane_b32 s9, v248, 21
	v_lshl_add_u64 v[10:11], v[8:9], 0, v[2:3]
	s_nop 3
	global_load_dword v113, v4, s[8:9]
	s_nop 0
	global_load_dwordx4 v[2:5], v[10:11], off
	s_lshl_b64 s[0:1], s[0:1], 1
	v_readlane_b32 s8, v248, 7
	v_readlane_b32 s9, v248, 8
	s_add_u32 s0, s8, s0
	v_cmp_gt_i32_e32 vcc, 2, v21
	v_bfe_u32 v21, v30, 3, 3
	s_addc_u32 s1, s9, s1
	v_or_b32_e32 v21, v20, v21
	v_bfe_u32 v18, v30, 4, 2
	s_add_u32 s0, s0, s10
	v_or_b32_e32 v28, 8, v21
	s_addc_u32 s1, s1, 0
	v_cndmask_b32_e64 v102, v22, 0, vcc
	v_bitop3_b32 v24, v18, v30, 7 bitop3:0x78
	v_lshrrev_b32_e32 v22, 1, v28
	v_lshlrev_b32_e32 v98, 10, v21
	v_xor_b32_e32 v25, v22, v30
	v_lshl_add_u64 v[22:23], s[0:1], 0, v[98:99]
	v_lshlrev_b32_e32 v98, 4, v24
	v_lshl_add_u64 v[104:105], v[22:23], 0, v[98:99]
	v_lshlrev_b32_e32 v22, 10, v28
	v_mov_b32_e32 v23, v99
	v_lshlrev_b32_e32 v24, 4, v25
	v_or_b32_e32 v6, 64, v6
	v_readfirstlane_b32 s8, v31
	v_lshl_add_u64 v[22:23], s[0:1], 0, v[22:23]
	v_and_b32_e32 v24, 0x70, v24
	v_mov_b32_e32 v25, v99
	v_ashrrev_i32_e32 v7, 31, v6
	v_lshl_add_u64 v[106:107], v[22:23], 0, v[24:25]
	v_mov_b64_e32 v[22:23], s[6:7]
	s_movk_i32 s6, 0x4200
	s_lshl_b32 s25, s8, 11
	v_lshlrev_b64 v[6:7], 10, v[6:7]
	v_mad_u64_u32 v[26:27], s[0:1], v21, s6, v[22:23]
	v_mad_u64_u32 v[22:23], s[0:1], v28, s6, v[22:23]
	v_ashrrev_i32_e32 v103, 31, v102
	v_add_u32_e32 v21, s25, v114
	v_lshl_add_u64 v[14:15], v[8:9], 0, v[6:7]
	v_lshl_add_u64 v[108:109], v[26:27], 0, v[98:99]
	v_lshl_add_u64 v[110:111], v[22:23], 0, v[24:25]
	v_lshlrev_b64 v[22:23], 10, v[102:103]
	v_readfirstlane_b32 s0, v21
	v_add_u32_e32 v26, 0x400, v21
	global_load_dwordx4 v[6:9], v[10:11], off offset:64
	s_nop 0
	global_load_dwordx4 v[10:13], v[14:15], off
	s_nop 0
	global_load_dwordx4 v[14:17], v[14:15], off offset:64
	s_waitcnt lgkmcnt(0)
	s_nop 0
	v_lshl_add_u64 v[24:25], v[104:105], 0, v[22:23]
	s_mov_b32 m0, s0
	v_readfirstlane_b32 s0, v26
	global_load_lds_dwordx4 v[24:25], off
	v_lshl_add_u64 v[24:25], v[106:107], 0, v[22:23]
	s_mov_b32 m0, s0
	v_add_u32_e32 v28, 0x6000, v21
	global_load_lds_dwordx4 v[24:25], off
	v_lshlrev_b64 v[24:25], 1, v[102:103]
	v_readfirstlane_b32 s0, v28
	v_add_u32_e32 v28, 0x6400, v21
	v_lshl_add_u64 v[26:27], v[108:109], 0, v[24:25]
	s_mov_b32 m0, s0
	v_readfirstlane_b32 s0, v28
	global_load_lds_dwordx4 v[26:27], off
	s_mov_b32 m0, s0
	s_mov_b64 s[0:1], 0x10000
	v_add_u32_e32 v32, 0x2000, v21
	v_lshl_add_u64 v[24:25], v[110:111], 0, v[24:25]
	v_lshl_add_u64 v[22:23], v[22:23], 0, s[0:1]
	v_readfirstlane_b32 s0, v32
	global_load_lds_dwordx4 v[24:25], off
	v_lshl_add_u64 v[28:29], v[104:105], 0, v[22:23]
	s_mov_b32 m0, s0
	v_lshl_add_u64 v[22:23], v[106:107], 0, v[22:23]
	global_load_lds_dwordx4 v[28:29], off
	v_add_u32_e32 v28, 0x2400, v21
	s_mov_b64 s[6:7], 0x80
	v_readfirstlane_b32 s0, v28
	s_mov_b32 m0, s0
	v_and_b32_e32 v103, 63, v30
	global_load_lds_dwordx4 v[22:23], off
	v_lshl_add_u64 v[22:23], v[26:27], 0, s[6:7]
	v_add_u32_e32 v26, 0x8000, v21
	v_add_u32_e32 v21, 0x8400, v21
	v_readfirstlane_b32 s0, v26
	s_mov_b32 m0, s0
	v_readfirstlane_b32 s0, v21
	global_load_lds_dwordx4 v[22:23], off
	v_lshl_add_u64 v[22:23], v[24:25], 0, s[6:7]
	s_mov_b32 m0, s0
	s_mul_i32 s6, s5, 0x1d1
	global_load_lds_dwordx4 v[22:23], off
	v_and_b32_e32 v23, 0xff, v30
	v_add_u32_e32 v22, -16, v103
	s_add_i32 s6, s6, -16
	v_mul_u32_u24_e32 v24, 31, v31
	v_lshlrev_b32_e32 v21, 3, v18
	v_cmp_gt_u32_e64 s[0:1], 31, v22
	v_lshl_add_u32 v22, v23, 2, v117
	v_add3_u32 v98, s6, v24, v103
	v_or_b32_e32 v23, 0xffffff00, v23
	v_mov_b32_e32 v26, 0
	v_mov_b32_e32 v27, 0
	v_mov_b32_e32 v28, 0
	v_mov_b32_e32 v29, 0
	v_and_b32_e32 v32, 0xff, v30
	s_movk_i32 s8, 0xc0
	v_lshl_add_u64 v[24:25], v[98:99], 2, s[80:81]
	v_cmp_gt_u32_e64 s[8:9], s8, v32
	s_and_saveexec_b64 s[6:7], s[0:1]
	global_load_dword v26, v[24:25], off
	global_load_dword v27, v[24:25], off offset:496
	global_load_dword v28, v[24:25], off offset:992
	s_and_b64 exec, exec, s[8:9]
	global_load_dword v29, v[24:25], off offset:1488
	s_mov_b64 exec, s[6:7]
	s_waitcnt vmcnt(0)
; #define LAS __attribute__((address_space(3)))
; template <bool ISA>
; __device__ __forceinline__ void attn_unit(const Params& p, unsigned char* smem, int b, int hh, int blk) {
;     ...
;         const float l0 = ISA ? __builtin_amdgcn_exp2f(p.sink[hh] * L2E - M2) : 0.f;
;         osum[q] = (f32x4){l0, l0, l0, l0};
; #pragma unroll
;         for (int df = 0; df < 4; ++df) o[q][df] = (f32x4){0.f, 0.f, 0.f, 0.f};
;     }
;     const int qcol = wid * 16 + l15;
;     int cs = wid * 16 - 8; cs = cs < 0 ? 0 : (cs > 32 ? 32 : cs);
;     int wstart = qcol - 8; wstart = wstart < 0 ? 0 : (wstart > 48 ? 48 : wstart);
;     NaConst nc;
; #pragma unroll
;     for (int j = 0; j < 4; ++j) {
;         const int kc = cs + (j >> 1) * 16 + gq * 4 + (j & 1) * 2;
;         nc.cm[j] = (((kc >= wstart) && (kc < wstart + 16)) ? 0xFFFFu : 0u) | (((kc + 1 >= wstart) && (kc + 1 < wstart + 16)) ? 0xFFFF0000u : 0u);
;     }
;     nc.blane = (unsigned)(size_t)(LAS unsigned char*)smem + 49152u + (unsigned)((16 + (cs + gq * 4 - qcol + 15)) * 4);
;     LAS unsigned char* ldsu = (LAS unsigned char*)smem;
;     const unsigned ldsa = (unsigned)(size_t)ldsu;
;     const int wuni = __builtin_amdgcn_readfirstlane(wid);
;     const bf16_t* kp0; const bf16_t* kp1; const bf16_t* vp0; const bf16_t* vp1;
;     {
;         const int ra = (wid * 2) * 8 + (lane >> 3), rb = (wid * 2 + 1) * 8 + (lane >> 3);
;         const int ca = ((lane & 7) ^ ((ra >> 1) & 7)) * 8, cb = ((lane & 7) ^ ((rb >> 1) & 7)) * 8;
;         kp0 = kbase + (size_t)ra * ldk + ca; kp1 = kbase + (size_t)rb * ldk + cb;
;         vp0 = vbase + (size_t)ra * TT + ca; vp1 = vbase + (size_t)rb * TT + cb;
;     }
;     ...
;     asm volatile("s_waitcnt lgkmcnt(0)" ::: "memory"); __builtin_amdgcn_s_barrier(); asm volatile("" ::: "memory");
;     ADMA(0);
;     if (ntile > 1) ADMA(1);
;     if (!ISA) {
;         for (int i = tid; i < 15 * 64; i += 256) { const int dr = i >> 6, dc = (i & 63) - 16; rpbl[i] = ((dc >= 0 && dc < 31) ? p.rpb[hh * 465 + dr * 31 + dc] * L2E : 0.f) - M2; }
;     }
	v_mul_f32_e32 v26, 0x3fb8aa3b, v26
	v_mul_f32_e32 v27, 0x3fb8aa3b, v27
	v_mul_f32_e32 v28, 0x3fb8aa3b, v28
	v_mul_f32_e32 v29, 0x3fb8aa3b, v29
	v_sub_f32_e32 v26, v26, v113
	v_sub_f32_e32 v27, v27, v113
	v_sub_f32_e32 v28, v28, v113
	v_sub_f32_e32 v29, v29, v113
	ds_write_b32 v22, v26
	ds_write_b32 v22, v27 offset:1024
	ds_write_b32 v22, v28 offset:2048
	s_and_saveexec_b64 s[6:7], s[8:9]
	ds_write_b32 v22, v29 offset:3072
	s_or_b64 exec, exec, s[6:7]
	v_or_b32_e32 v22, v20, v112
	v_med3_u32 v20, v20, 8, 40
	v_add_u32_e32 v20, -8, v20
	v_med3_u32 v23, v22, 8, 56
	v_lshlrev_b32_e32 v98, 2, v18
	v_add_u32_e32 v24, v20, v98
	v_add_u32_e32 v25, 8, v23
	v_add_u32_e32 v23, -8, v23
	v_cmp_lt_u32_e64 s[0:1], v24, v25
	v_or_b32_e32 v26, 1, v24
	v_cmp_ge_u32_e64 s[20:21], v24, v23
	v_cmp_lt_u32_e64 s[6:7], v26, v25
	v_add_u32_e32 v29, 16, v24
	s_and_b64 s[0:1], s[20:21], s[0:1]
	v_cmp_ge_u32_e64 s[20:21], v26, v23
	v_or_b32_e32 v27, 2, v24
	v_or_b32_e32 v28, 3, v24
	v_add_u32_e32 v30, 17, v24
	v_or_b32_e32 v31, 2, v29
	v_add_u32_e32 v32, 19, v24
	s_and_b64 s[6:7], s[20:21], s[6:7]
	v_cmp_lt_u32_e64 s[8:9], v27, v25
	v_cmp_lt_u32_e64 s[10:11], v28, v25
	v_cmp_lt_u32_e64 s[12:13], v29, v25
	v_cmp_lt_u32_e64 s[14:15], v30, v25
	v_cmp_lt_u32_e64 s[16:17], v31, v25
	v_cmp_lt_u32_e64 s[18:19], v32, v25
	v_cndmask_b32_e64 v25, 0, v119, s[6:7]
	v_cmp_ge_u32_e64 s[6:7], v27, v23
	s_and_b64 s[6:7], s[6:7], s[8:9]
	v_cmp_ge_u32_e64 s[8:9], v28, v23
	s_and_b64 s[8:9], s[8:9], s[10:11]
	v_cmp_ge_u32_e64 s[10:11], v30, v23
	v_cndmask_b32_e64 v26, 0, v119, s[8:9]
	v_cmp_ge_u32_e64 s[8:9], v29, v23
	s_and_b64 s[10:11], s[10:11], s[14:15]
	v_cndmask_b32_e64 v28, 0, v120, s[0:1]
	s_and_b64 s[8:9], s[8:9], s[12:13]
	v_cndmask_b32_e64 v27, 0, v119, s[10:11]
	v_cmp_ge_u32_e64 s[10:11], v31, v23
	v_cmp_ge_u32_e64 s[12:13], v32, v23
	v_or_b32_e32 v125, v25, v28
	v_cndmask_b32_e64 v25, 0, v120, s[6:7]
	v_sub_u32_e32 v22, v24, v22
	s_and_b64 s[10:11], s[10:11], s[16:17]
	s_and_b64 s[12:13], s[12:13], s[18:19]
	v_or_b32_e32 v126, v26, v25
	v_cndmask_b32_e64 v25, 0, v120, s[8:9]
	v_min_i32_e32 v19, 0x78, v19
	v_cndmask_b32_e64 v23, 0, v119, s[12:13]
	v_or_b32_e32 v127, v27, v25
	v_cndmask_b32_e64 v25, 0, v120, s[10:11]
	v_lshl_add_u32 v129, v22, 2, v115
	v_lshrrev_b32_e32 v22, 1, v112
	v_cndmask_b32_e64 v137, v19, 0, vcc
	v_med3_i32 v19, v101, 3, v121
	v_or_b32_e32 v128, v25, v23
	v_xor_b32_e32 v25, v18, v22
	v_add_u32_e32 v138, -3, v19
	v_add_u32_e32 v140, 5, v19
	v_add_u16_e32 v19, v20, v112
	v_lshlrev_b32_e32 v131, 4, v25
	v_bitop3_b32 v25, v18, v22, 4 bitop3:0x36
	v_lshrrev_b16_e32 v19, 1, v19
	v_or_b32_e32 v23, 4, v18
	v_lshlrev_b32_e32 v132, 4, v25
	v_lshrrev_b32_e32 v25, 5, v103
	v_bitop3_b32 v18, v19, v18, 7 bitop3:0x6c
	v_xor_b32_e32 v26, v25, v22
	v_lshlrev_b32_e32 v142, 4, v18
	v_bitop3_b32 v18, v19, v23, 7 bitop3:0x6c
	v_lshlrev_b32_e32 v130, 7, v112
	v_and_b32_e32 v21, 8, v21
	v_lshlrev_b32_e32 v26, 4, v26
	v_lshlrev_b32_e32 v143, 4, v18
	v_lshrrev_b32_e32 v18, 3, v24
	v_or3_b32 v134, v26, v130, v21
	v_bitop3_b32 v26, v25, v22, 2 bitop3:0x36
	v_xor_b32_e32 v18, v18, v22
	v_lshlrev_b32_e32 v135, 4, v26
	v_bitop3_b32 v26, v25, v22, 4 bitop3:0x36
	v_lshlrev_b32_e32 v144, 4, v18
	v_lshlrev_b32_e32 v18, 1, v24
	v_lshlrev_b32_e32 v26, 4, v26
	v_and_or_b32 v145, v18, 8, v130
	v_lshrrev_b32_e32 v18, 3, v29
	v_or_b32_e32 v133, v21, v130
	v_bitop3_b32 v25, v25, v22, 6 bitop3:0x36
	v_add_lshl_u32 v141, v20, v112, 7
	v_xor_b32_e32 v18, v18, v22
	v_or3_b32 v147, v130, v26, v21
	v_mov_b32_e32 v20, v99
	v_mov_b32_e32 v21, v99
	v_lshlrev_b32_e32 v136, 4, v25
	v_lshlrev_b32_e32 v146, 4, v18
	v_mov_b32_e32 v18, v99
	v_mov_b32_e32 v19, v99
	v_mov_b32_e32 v50, 0
	v_mov_b64_e32 v[24:25], v[20:21]
	v_mov_b64_e32 v[28:29], v[20:21]
	v_mov_b64_e32 v[32:33], v[20:21]
	v_mov_b64_e32 v[36:37], v[20:21]
	v_mov_b64_e32 v[40:41], v[20:21]
	v_mov_b64_e32 v[44:45], v[20:21]
	v_mov_b64_e32 v[48:49], v[20:21]
	s_mov_b32 s26, 2
	v_add_u32_e32 v139, 8, v137
	s_movk_i32 s8, 0x1e40
	v_mov_b64_e32 v[22:23], v[18:19]
	v_mov_b64_e32 v[26:27], v[18:19]
	v_mov_b64_e32 v[30:31], v[18:19]
	v_mov_b64_e32 v[34:35], v[18:19]
	v_mov_b64_e32 v[38:39], v[18:19]
	v_mov_b64_e32 v[42:43], v[18:19]
	v_mov_b64_e32 v[46:47], v[18:19]
	v_mov_b32_e32 v51, v50
	v_mov_b32_e32 v52, v50
	v_mov_b32_e32 v53, v50
	v_mov_b32_e32 v54, v50
	v_mov_b32_e32 v55, v50
	v_mov_b32_e32 v56, v50
	v_mov_b32_e32 v57, v50
	s_cmpk_eq_i32 s8, 0x2140
	s_mov_b64 s[0:1], -1
	s_cbranch_scc1 .LBB0_386
